# MLA QK^T phase: softmax VALU stream starts at gap 5 (first four gaps MFMA + K reads + DMA only)
# baseline (speedup 1.0000x reference)
.Lmla_rope1:
	ds_read_b128 v[190:193], v156 offset:4608
	v_mfma_f32_32x32x16_bf16 v[100:115], v[194:197], v[132:135], v[100:115]
	s_add_i32 s8, s27, 1
	s_min_i32 s8, s8, s2
	s_lshl_b32 s8, s8, 17
	v_lshl_add_u64 v[154:155], v[178:179], 0, s[8:9]
	s_add_i32 s8, s14, 0xffffe000
	s_and_b32 s15, s8, 0x6000
	s_add_i32 s8, s26, s15
	v_lshl_add_u64 v[154:155], v[154:155], 0, s[24:25]
	s_add_i32 m0, s8, 0xc000
	s_nop 0
	global_load_lds_dwordx4 v[154:155], off
	ds_read_b128 v[194:197], v156 offset:6144
	v_mfma_f32_32x32x16_bf16 v[84:99], v[198:201], v[132:135], v[84:99]
	ds_read_b128 v[198:201], v156 offset:6656
	s_waitcnt lgkmcnt(0)
	v_mfma_f32_32x32x16_bf16 v[100:115], v[202:205], v[128:131], v[100:115]
	ds_read_b128 v[202:205], v156 offset:8192
	v_exp_f32_e32 v60, v60
	v_exp_f32_e32 v61, v61
	v_exp_f32_e32 v62, v62
	v_exp_f32_e32 v63, v63
	v_exp_f32_e32 v64, v64
	v_mfma_f32_32x32x16_bf16 v[84:99], v[190:193], v[128:131], v[84:99]
	ds_read_b128 v[190:193], v156 offset:8704
	v_exp_f32_e32 v65, v65
	v_exp_f32_e32 v66, v66
	v_exp_f32_e32 v67, v67
	v_add_f32_e32 v162, v68, v69
	ds_read_b64_tr_b16 v[172:173], v157 offset:49152
	ds_read_b64_tr_b16 v[174:175], v157 offset:49664
	v_mfma_f32_32x32x16_bf16 v[100:115], v[194:197], v[124:127], v[100:115]
	ds_read_b128 v[194:197], v156 offset:10240
	v_add_f32_e32 v161, v70, v162
	v_add_f32_e32 v161, v71, v161
	v_add_f32_e32 v161, v72, v161
	v_add_f32_e32 v144, v73, v161
	v_cvt_pk_bf16_f32 v140, v68, v69
	v_cvt_pk_bf16_f32 v141, v70, v71
	ds_read_b64_tr_b16 v[68:69], v157 offset:53248
	ds_read_b64_tr_b16 v[70:71], v157 offset:53760
	v_add_f32_e32 v142, v74, v144
	v_mfma_f32_32x32x16_bf16 v[84:99], v[198:201], v[124:127], v[84:99]
	ds_read_b128 v[198:201], v156 offset:10752
	v_add_f32_e32 v142, v75, v142
	v_add_f32_e32 v142, v76, v142
	v_add_f32_e32 v144, v77, v142
	v_cvt_pk_bf16_f32 v142, v72, v73
	v_cvt_pk_bf16_f32 v143, v74, v75
	ds_read_b64_tr_b16 v[72:73], v157 offset:50176
	ds_read_b64_tr_b16 v[74:75], v157 offset:50688
	v_add_f32_e32 v144, v78, v144
	v_add_f32_e32 v144, v79, v144
	s_waitcnt lgkmcnt(0)
	v_mfma_f32_32x32x16_bf16 v[100:115], v[202:205], v[120:123], v[100:115]
	v_add_f32_e32 v144, v80, v144
	v_add_f32_e32 v148, v81, v144
	v_cvt_pk_bf16_f32 v144, v76, v77
	v_cvt_pk_bf16_f32 v145, v78, v79
	ds_read_b64_tr_b16 v[76:77], v157 offset:54272
	ds_read_b64_tr_b16 v[78:79], v157 offset:54784
	v_add_f32_e32 v146, v82, v148
	v_add_f32_e32 v146, v83, v146
	v_add_f32_e32 v146, v52, v146
	v_add_f32_e32 v148, v53, v146
	v_cvt_pk_bf16_f32 v146, v80, v81
	v_mfma_f32_32x32x16_bf16 v[84:99], v[190:193], v[120:123], v[84:99]
	v_cvt_pk_bf16_f32 v147, v82, v83
	ds_read_b64_tr_b16 v[80:81], v157 offset:51200
	ds_read_b64_tr_b16 v[82:83], v157 offset:51712
	v_add_f32_e32 v148, v54, v148
	v_add_f32_e32 v148, v55, v148
	v_add_f32_e32 v148, v56, v148
	v_add_f32_e32 v152, v57, v148
	v_cvt_pk_bf16_f32 v148, v52, v53
	v_cvt_pk_bf16_f32 v149, v54, v55
	ds_read_b64_tr_b16 v[52:53], v157 offset:55296
	ds_read_b64_tr_b16 v[54:55], v157 offset:55808
	v_mfma_f32_32x32x16_bf16 v[100:115], v[194:197], v[116:119], v[100:115]
	v_add_f32_e32 v150, v58, v152
	v_add_f32_e32 v150, v59, v150
	v_add_f32_e32 v150, v60, v150
	v_add_f32_e32 v152, v61, v150
	v_cvt_pk_bf16_f32 v150, v56, v57
	v_cvt_pk_bf16_f32 v151, v58, v59
	ds_read_b64_tr_b16 v[56:57], v157 offset:52224
	ds_read_b64_tr_b16 v[58:59], v157 offset:52736
	v_add_f32_e32 v152, v62, v152
	v_add_f32_e32 v152, v63, v152
	v_add_f32_e32 v152, v64, v152
	v_mfma_f32_32x32x16_bf16 v[84:99], v[198:201], v[116:119], v[84:99]
	v_add_f32_e32 v160, v65, v152
	v_cvt_pk_bf16_f32 v152, v60, v61
	v_cvt_pk_bf16_f32 v153, v62, v63
	ds_read_b64_tr_b16 v[60:61], v157 offset:56320
	ds_read_b64_tr_b16 v[62:63], v157 offset:56832
	v_add_f32_e32 v154, v66, v160
	v_add_f32_e32 v156, v67, v154
	v_cvt_pk_bf16_f32 v154, v64, v65
	v_cvt_pk_bf16_f32 v155, v66, v67
	s_setprio 0
	s_cmp_lt_i32 s19, s52
	s_cbranch_scc0 .LBB0_1167

.Lmla_rope2:
	ds_read_b128 v[190:193], v140 offset:4608
	v_mfma_f32_32x32x16_bf16 v[68:83], v[194:197], v[132:135], v[68:83]
	s_cmp_lt_u32 s19, s3
	s_cselect_b32 s8, s16, s2
	s_lshl_b64 s[10:11], s[8:9], 17
	v_lshl_add_u64 v[170:171], v[178:179], 0, s[10:11]
	s_add_i32 s8, s26, s17
	v_lshl_add_u64 v[170:171], v[170:171], 0, s[24:25]
	s_add_i32 m0, s8, 0xc000
	s_and_b32 s17, s27, 3
	global_load_lds_dwordx4 v[170:171], off
	s_mulk_i32 s17, 0x3000
	ds_read_b128 v[194:197], v140 offset:6144
	v_mfma_f32_32x32x16_bf16 v[52:67], v[198:201], v[132:135], v[52:67]
	ds_read_b128 v[198:201], v140 offset:6656
	s_waitcnt lgkmcnt(0)
	v_mfma_f32_32x32x16_bf16 v[68:83], v[202:205], v[128:131], v[68:83]
	ds_read_b128 v[202:205], v140 offset:8192
	v_exp_f32_e32 v92, v92
	v_exp_f32_e32 v93, v93
	v_exp_f32_e32 v94, v94
	v_exp_f32_e32 v95, v95
	v_exp_f32_e32 v96, v96
	v_mfma_f32_32x32x16_bf16 v[52:67], v[190:193], v[128:131], v[52:67]
	ds_read_b128 v[190:193], v140 offset:8704
	v_exp_f32_e32 v97, v97
	v_exp_f32_e32 v98, v98
	v_exp_f32_e32 v99, v99
	v_add_f32_e32 v147, v100, v101
	ds_read_b64_tr_b16 v[172:173], v141 offset:49152
	ds_read_b64_tr_b16 v[174:175], v141 offset:49664
	v_mfma_f32_32x32x16_bf16 v[68:83], v[194:197], v[124:127], v[68:83]
	ds_read_b128 v[194:197], v140 offset:10240
	v_add_f32_e32 v146, v102, v147
	v_add_f32_e32 v146, v103, v146
	v_add_f32_e32 v146, v104, v146
	v_add_f32_e32 v144, v105, v146
	v_cvt_pk_bf16_f32 v156, v100, v101
	v_cvt_pk_bf16_f32 v157, v102, v103
	ds_read_b64_tr_b16 v[100:101], v141 offset:53248
	ds_read_b64_tr_b16 v[102:103], v141 offset:53760
	v_add_f32_e32 v144, v106, v144
	v_mfma_f32_32x32x16_bf16 v[52:67], v[198:201], v[124:127], v[52:67]
	ds_read_b128 v[198:201], v140 offset:10752
	v_add_f32_e32 v144, v107, v144
	v_add_f32_e32 v144, v108, v144
	v_add_f32_e32 v144, v109, v144
	v_cvt_pk_bf16_f32 v158, v104, v105
	v_cvt_pk_bf16_f32 v159, v106, v107
	ds_read_b64_tr_b16 v[104:105], v141 offset:50176
	ds_read_b64_tr_b16 v[106:107], v141 offset:50688
	v_add_f32_e32 v144, v110, v144
	v_add_f32_e32 v144, v111, v144
	s_waitcnt lgkmcnt(0)
	v_mfma_f32_32x32x16_bf16 v[68:83], v[202:205], v[120:123], v[68:83]
	v_add_f32_e32 v144, v112, v144
	v_add_f32_e32 v144, v113, v144
	v_cvt_pk_bf16_f32 v160, v108, v109
	v_cvt_pk_bf16_f32 v161, v110, v111
	ds_read_b64_tr_b16 v[108:109], v141 offset:54272
	ds_read_b64_tr_b16 v[110:111], v141 offset:54784
	v_add_f32_e32 v144, v114, v144
	v_add_f32_e32 v144, v115, v144
	v_add_f32_e32 v144, v84, v144
	v_add_f32_e32 v144, v85, v144
	v_cvt_pk_bf16_f32 v162, v112, v113
	v_mfma_f32_32x32x16_bf16 v[52:67], v[190:193], v[120:123], v[52:67]
	v_cvt_pk_bf16_f32 v163, v114, v115
	ds_read_b64_tr_b16 v[112:113], v141 offset:51200
	ds_read_b64_tr_b16 v[114:115], v141 offset:51712
	v_add_f32_e32 v144, v86, v144
	v_add_f32_e32 v144, v87, v144
	v_add_f32_e32 v144, v88, v144
	v_add_f32_e32 v144, v89, v144
	v_cvt_pk_bf16_f32 v164, v84, v85
	v_cvt_pk_bf16_f32 v165, v86, v87
	ds_read_b64_tr_b16 v[84:85], v141 offset:55296
	ds_read_b64_tr_b16 v[86:87], v141 offset:55808
	v_mfma_f32_32x32x16_bf16 v[68:83], v[194:197], v[116:119], v[68:83]
	v_add_f32_e32 v144, v90, v144
	v_add_f32_e32 v144, v91, v144
	v_add_f32_e32 v144, v92, v144
	v_add_f32_e32 v144, v93, v144
	v_cvt_pk_bf16_f32 v166, v88, v89
	v_cvt_pk_bf16_f32 v167, v90, v91
	ds_read_b64_tr_b16 v[88:89], v141 offset:52224
	ds_read_b64_tr_b16 v[90:91], v141 offset:52736
	v_add_f32_e32 v144, v94, v144
	v_add_f32_e32 v144, v95, v144
	v_add_f32_e32 v144, v96, v144
	v_mfma_f32_32x32x16_bf16 v[52:67], v[198:201], v[116:119], v[52:67]
	v_add_f32_e32 v144, v97, v144
	v_cvt_pk_bf16_f32 v168, v92, v93
	v_cvt_pk_bf16_f32 v169, v94, v95
	ds_read_b64_tr_b16 v[92:93], v141 offset:56320
	ds_read_b64_tr_b16 v[94:95], v141 offset:56832
	v_add_f32_e32 v140, v98, v144
	v_add_f32_e32 v140, v99, v140
	v_cvt_pk_bf16_f32 v170, v96, v97
	v_cvt_pk_bf16_f32 v171, v98, v99
	s_setprio 0
	s_cmp_lt_i32 s27, s52
	s_cbranch_scc0 .LBB0_1171
